# MoE combine: second half-rows touched early with throw-away loads so their real loads hit L2
# baseline (speedup 1.0000x reference)
; __device__ __forceinline__ void unpack8(const u32x4& w, f32x4& a, f32x4& b) { a = (f32x4){bf_lo(w.x), bf_hi(w.x), bf_lo(w.y), bf_hi(w.y)}; b = (f32x4){bf_lo(w.z), bf_hi(w.z), bf_lo(w.w), bf_hi(w.w)}; }
; __device__ __forceinline__ void phase_moe_combine(const Frame& F, const Params& P, bool dry) {
;     ...
;     for (int t0 = gw; t0 < NTOK; t0 += 4 * NGW) {
;         int s0[4], s1[4]; float g0[4], g1[4];
; #pragma unroll
;         for (int k = 0; k < 4; ++k) { const int tok = t0 + k * NGW; const int tk = tok < NTOK ? tok : 0; s0[k] = tokslot[tk * 2]; s1[k] = tokslot[tk * 2 + 1]; g0[k] = topg[tk * 2]; g1[k] = topg[tk * 2 + 1]; }
; #pragma unroll
;         for (int q = 0; q < 2; ++q) { const int c = (q * 64 + lane) * 8; u32x4 w0[4], w1[4], wx[4];
; #pragma unroll
;             for (int k = 0; k < 4; ++k) { const int tok = t0 + k * NGW; const int tk = tok < NTOK ? tok : 0; w0[k] = *(const u32x4*)(Y + (size_t)s0[k] * D + c); w1[k] = *(const u32x4*)(Y + (size_t)s1[k] * D + c); wx[k] = *(const u32x4*)(XB + (size_t)tk * D + c); }
; #pragma unroll
;             for (int k = 0; k < 4; ++k) { const int tok = t0 + k * NGW; if (tok >= NTOK) continue;
;                 f32x4 a0, a1, b0, b1, x0, x1; unpack8(w0[k], a0, a1); unpack8(w1[k], b0, b1); unpack8(wx[k], x0, x1); f32x4* o = (f32x4*)(out + (size_t)tok * D + c);
;                 const f32x4 r0 = x0 + a0 * g0[k] + b0 * g1[k], r1 = x1 + a1 * g0[k] + b1 * g1[k]; if (!dry) { o[0] = r0; o[1] = r1; } } } }
.LBB0_1683:
	s_add_i32 s6, s0, -1
	s_ashr_i32 s7, s6, 31
	s_lshl_b64 s[2:3], s[6:7], 2
	s_add_u32 s4, s20, s2
	s_addc_u32 s5, s21, s3
	v_mov_b64_e32 v[0:1], s[4:5]
	flat_load_dword v0, v[0:1]
	s_ashr_i32 s1, s0, 31
	s_lshl_b64 s[4:5], s[0:1], 2
	s_add_u32 s8, s20, s4
	s_addc_u32 s9, s21, s5
	s_add_u32 s2, s22, s2
	s_addc_u32 s3, s23, s3
	v_mov_b64_e32 v[4:5], s[2:3]
	s_add_u32 s2, s22, s4
	v_mov_b64_e32 v[2:3], s[8:9]
	s_addc_u32 s3, s23, s5
	flat_load_dword v2, v[2:3]
	s_mul_i32 s7, s78, 48
	flat_load_dword v64, v[4:5]
	v_mov_b64_e32 v[4:5], s[2:3]
	s_mul_i32 s2, s78, 24
	s_add_i32 s1, s76, s24
	s_add_i32 s3, s6, s81
	s_add_i32 s4, s81, s24
	s_add_i32 s5, s6, s86
	s_add_i32 s2, s2, s24
	s_add_i32 s6, s6, s7
	s_cmp_lt_i32 s2, 0x8000
	s_cselect_b32 s12, s6, 0
	s_cselect_b32 s10, s2, 0
	s_cmp_lt_i32 s4, 0x8000
	s_cselect_b32 s16, s5, 0
	s_cselect_b32 s14, s4, 0
	s_cmp_lt_i32 s1, 0x8000
	s_cselect_b64 s[6:7], -1, 0
	s_and_b64 s[8:9], s[6:7], exec
	s_cselect_b32 s18, s3, 0
	s_cselect_b32 s8, s1, 0
	s_ashr_i32 s19, s18, 31
	s_lshl_b64 s[26:27], s[18:19], 2
	s_add_u32 s18, s20, s26
	s_addc_u32 s19, s21, s27
	s_add_u32 s26, s22, s26
	s_addc_u32 s27, s23, s27
	s_ashr_i32 s17, s16, 31
	flat_load_dword v66, v[4:5]
	s_movk_i32 s3, 0xfc00
	v_add_co_u32_e32 v36, vcc, s3, v54
	s_waitcnt vmcnt(0) lgkmcnt(0)
	v_ashrrev_i32_e32 v1, 31, v0
	v_lshlrev_b64 v[68:69], 11, v[0:1]
	v_mov_b64_e32 v[0:1], s[18:19]
	flat_load_dwordx2 v[0:1], v[0:1]
	v_mov_b64_e32 v[4:5], s[26:27]
	s_lshl_b64 s[26:27], s[16:17], 2
	s_add_u32 s16, s20, s26
	s_addc_u32 s17, s21, s27
	s_add_u32 s26, s22, s26
	s_addc_u32 s27, s23, s27
	s_ashr_i32 s13, s12, 31
	flat_load_dwordx2 v[62:63], v[4:5]
	v_mov_b64_e32 v[4:5], s[26:27]
	s_lshl_b64 s[26:27], s[12:13], 2
	s_add_u32 s12, s20, s26
	s_addc_u32 s13, s21, s27
	v_mov_b64_e32 v[20:21], s[12:13]
	flat_load_dwordx2 v[60:61], v[4:5]
	v_ashrrev_i32_e32 v3, 31, v2
	flat_load_dwordx2 v[20:21], v[20:21]
	s_add_u32 s26, s22, s26
	s_addc_u32 s27, s23, s27
	v_lshlrev_b64 v[70:71], 11, v[2:3]
	v_mov_b64_e32 v[4:5], s[26:27]
	flat_load_dwordx2 v[58:59], v[4:5]
	v_mov_b64_e32 v[12:13], s[16:17]
	s_ashr_i32 s9, s8, 31
	s_lshl_b64 s[8:9], s[8:9], 11
	s_ashr_i32 s15, s14, 31
	v_addc_co_u32_e32 v37, vcc, -1, v55, vcc
	v_lshl_add_u64 v[40:41], v[44:45], 0, v[70:71]
	v_lshl_add_u64 v[84:85], v[44:45], 0, v[68:69]
	s_lshl_b64 s[14:15], s[14:15], 11
	s_ashr_i32 s11, s10, 31
	flat_load_dwordx4 v[240:243], v[36:37] offset:1024
	flat_load_dwordx4 v[36:39], v[36:37]
	s_lshl_b64 s[16:17], s[10:11], 11
	flat_load_dwordx4 v[240:243], v[40:41] offset:1024
	flat_load_dwordx4 v[40:43], v[40:41]
	v_readlane_b32 s10, v254, 58
	flat_load_dwordx4 v[240:243], v[84:85] offset:1024
	flat_load_dwordx4 v[84:87], v[84:85]
	v_readlane_b32 s11, v254, 59
	s_cmpk_gt_i32 s1, 0x7fff
	flat_load_dwordx2 v[12:13], v[12:13]
	s_waitcnt vmcnt(0) lgkmcnt(0)
	v_ashrrev_i32_e32 v3, 31, v0
	v_mov_b32_e32 v2, v0
	v_lshlrev_b64 v[74:75], 11, v[2:3]
	v_ashrrev_i32_e32 v23, 31, v20
	v_mov_b32_e32 v22, v20
	v_lshlrev_b64 v[82:83], 11, v[22:23]
	v_ashrrev_i32_e32 v29, 31, v21
	v_mov_b32_e32 v28, v21
	v_lshl_add_u64 v[20:21], v[44:45], 0, v[82:83]
	flat_load_dwordx4 v[240:243], v[20:21] offset:1024
	flat_load_dwordx4 v[32:35], v[20:21]
	v_ashrrev_i32_e32 v5, 31, v1
	v_mov_b32_e32 v4, v1
	v_lshl_add_u64 v[0:1], v[44:45], 0, v[74:75]
	flat_load_dwordx4 v[240:243], v[0:1] offset:1024
	flat_load_dwordx4 v[8:11], v[0:1]
	v_lshlrev_b64 v[72:73], 11, v[4:5]
	v_lshl_add_u64 v[0:1], v[44:45], 0, v[72:73]
	flat_load_dwordx4 v[240:243], v[0:1] offset:1024
	flat_load_dwordx4 v[4:7], v[0:1]
	v_lshlrev_b64 v[80:81], 11, v[28:29]
	v_lshl_add_u64 v[20:21], v[44:45], 0, v[80:81]
	v_lshlrev_b32_e32 v98, 16, v38
	v_and_b32_e32 v99, 0xffff0000, v38
	v_lshlrev_b32_e32 v92, 16, v40
	v_and_b32_e32 v93, 0xffff0000, v40
	v_lshlrev_b32_e32 v88, 16, v84
	v_and_b32_e32 v89, 0xffff0000, v84
	v_lshlrev_b32_e32 v84, 16, v85
	v_and_b32_e32 v85, 0xffff0000, v85
	v_lshlrev_b32_e32 v94, 16, v41
	v_and_b32_e32 v95, 0xffff0000, v41
	v_lshlrev_b32_e32 v96, 16, v42
	v_and_b32_e32 v97, 0xffff0000, v42
	v_lshlrev_b32_e32 v40, 16, v43
	v_and_b32_e32 v41, 0xffff0000, v43
	v_lshlrev_b32_e32 v42, 16, v36
	v_and_b32_e32 v43, 0xffff0000, v36
	v_lshlrev_b32_e32 v36, 16, v37
	v_and_b32_e32 v37, 0xffff0000, v37
	v_lshlrev_b32_e32 v90, 16, v86
	v_and_b32_e32 v91, 0xffff0000, v86
	v_lshlrev_b32_e32 v86, 16, v87
	v_and_b32_e32 v87, 0xffff0000, v87
	v_lshlrev_b32_e32 v38, 16, v39
	v_and_b32_e32 v39, 0xffff0000, v39
	v_pk_fma_f32 v[42:43], v[64:65], v[88:89], v[42:43] op_sel_hi:[0,1,1]
	v_pk_fma_f32 v[36:37], v[64:65], v[84:85], v[36:37] op_sel_hi:[0,1,1]
	v_pk_fma_f32 v[90:91], v[64:65], v[90:91], v[98:99] op_sel_hi:[0,1,1]
	v_pk_fma_f32 v[38:39], v[64:65], v[86:87], v[38:39] op_sel_hi:[0,1,1]
	v_pk_fma_f32 v[86:87], v[66:67], v[94:95], v[36:37] op_sel_hi:[0,1,1]
	v_pk_fma_f32 v[84:85], v[66:67], v[92:93], v[42:43] op_sel_hi:[0,1,1]
	v_lshl_add_u64 v[36:37], v[56:57], 0, s[10:11]
	v_pk_fma_f32 v[40:41], v[66:67], v[40:41], v[38:39] op_sel_hi:[0,1,1]
	v_pk_fma_f32 v[38:39], v[66:67], v[96:97], v[90:91] op_sel_hi:[0,1,1]
	v_ashrrev_i32_e32 v15, 31, v12
	v_mov_b32_e32 v14, v12
	v_ashrrev_i32_e32 v17, 31, v13
	v_mov_b32_e32 v16, v13
	v_lshlrev_b64 v[78:79], 11, v[14:15]
	v_lshlrev_b64 v[76:77], 11, v[16:17]
	v_lshl_add_u64 v[12:13], v[44:45], 0, v[78:79]
	flat_load_dwordx4 v[240:243], v[12:13] offset:1024
	flat_load_dwordx4 v[24:27], v[12:13]
	v_lshl_add_u64 v[0:1], v[46:47], 0, s[8:9]
	v_lshl_add_u64 v[12:13], v[44:45], 0, v[76:77]
	flat_load_dwordx4 v[240:243], v[0:1] offset:1024
	flat_load_dwordx4 v[0:3], v[0:1]
	s_nop 0
	flat_load_dwordx4 v[240:243], v[12:13] offset:1024
	flat_load_dwordx4 v[16:19], v[12:13]
	v_lshl_add_u64 v[12:13], v[46:47], 0, s[14:15]
	flat_load_dwordx4 v[240:243], v[12:13] offset:1024
	flat_load_dwordx4 v[12:15], v[12:13]
	s_nop 0
	flat_load_dwordx4 v[240:243], v[20:21] offset:1024
	flat_load_dwordx4 v[28:31], v[20:21]
	v_lshl_add_u64 v[20:21], v[46:47], 0, s[16:17]
	flat_load_dwordx4 v[240:243], v[20:21] offset:1024
	flat_load_dwordx4 v[20:23], v[20:21]
	s_nop 0
	global_store_dwordx4 v[36:37], v[84:87], off
	global_store_dwordx4 v[36:37], v[38:41], off offset:16
	s_cbranch_scc1 .LBB0_1690
; __device__ __forceinline__ void unpack8(const u32x4& w, f32x4& a, f32x4& b) { a = (f32x4){bf_lo(w.x), bf_hi(w.x), bf_lo(w.y), bf_hi(w.y)}; b = (f32x4){bf_lo(w.z), bf_hi(w.z), bf_lo(w.w), bf_hi(w.w)}; }
; __device__ __forceinline__ void phase_moe_combine(const Frame& F, const Params& P, bool dry) {
;     ...
;             for (int k = 0; k < 4; ++k) { const int tok = t0 + k * NGW; if (tok >= NTOK) continue;
;                 f32x4 a0, a1, b0, b1, x0, x1; unpack8(w0[k], a0, a1); unpack8(w1[k], b0, b1); unpack8(wx[k], x0, x1); f32x4* o = (f32x4*)(out + (size_t)tok * D + c);
;                 const f32x4 r0 = x0 + a0 * g0[k] + b0 * g1[k], r1 = x1 + a1 * g0[k] + b1 * g1[k]; if (!dry) { o[0] = r0; o[1] = r1; } } } }
	s_waitcnt vmcnt(0) lgkmcnt(0)
	v_lshlrev_b32_e32 v40, 16, v10
	v_and_b32_e32 v41, 0xffff0000, v10
	v_lshlrev_b32_e32 v10, 16, v11
	v_and_b32_e32 v11, 0xffff0000, v11
	v_lshlrev_b32_e32 v86, 16, v0
	v_and_b32_e32 v87, 0xffff0000, v0
	v_lshlrev_b32_e32 v88, 16, v1
	v_and_b32_e32 v89, 0xffff0000, v1
	v_lshlrev_b32_e32 v0, 16, v2
	v_and_b32_e32 v1, 0xffff0000, v2
	v_lshlrev_b32_e32 v2, 16, v3
	v_and_b32_e32 v3, 0xffff0000, v3
	v_lshlrev_b32_e32 v38, 16, v8
	v_and_b32_e32 v39, 0xffff0000, v8
	v_lshlrev_b32_e32 v8, 16, v9
	v_and_b32_e32 v9, 0xffff0000, v9
	v_lshlrev_b32_e32 v84, 16, v6
	v_and_b32_e32 v85, 0xffff0000, v6
	v_lshlrev_b32_e32 v6, 16, v7
	v_and_b32_e32 v7, 0xffff0000, v7
	v_pk_fma_f32 v[2:3], v[62:63], v[10:11], v[2:3] op_sel_hi:[0,1,1]
	v_mov_b32_e32 v10, v63
	v_readlane_b32 s10, v255, 2
	v_lshlrev_b32_e32 v42, 16, v4
	v_and_b32_e32 v43, 0xffff0000, v4
	v_lshlrev_b32_e32 v4, 16, v5
	v_and_b32_e32 v5, 0xffff0000, v5
	v_pk_fma_f32 v[2:3], v[10:11], v[6:7], v[2:3] op_sel_hi:[0,1,1]
	v_pk_fma_f32 v[38:39], v[62:63], v[38:39], v[86:87] op_sel_hi:[0,1,1]
	v_pk_fma_f32 v[6:7], v[62:63], v[8:9], v[88:89] op_sel_hi:[0,1,1]
	v_readlane_b32 s11, v255, 3
	v_pk_fma_f32 v[0:1], v[62:63], v[40:41], v[0:1] op_sel_hi:[0,1,1]
	v_pk_fma_f32 v[6:7], v[10:11], v[4:5], v[6:7] op_sel_hi:[0,1,1]
	v_pk_fma_f32 v[4:5], v[10:11], v[42:43], v[38:39] op_sel_hi:[0,1,1]
	v_lshl_add_u64 v[8:9], v[56:57], 0, s[10:11]
	v_pk_fma_f32 v[0:1], v[10:11], v[84:85], v[0:1] op_sel_hi:[0,1,1]
	global_store_dwordx4 v[8:9], v[4:7], off
	global_store_dwordx4 v[8:9], v[0:3], off offset:16
	s_cmp_lt_i32 s4, 0x8000
	s_cselect_b64 s[10:11], -1, 0
	s_cmpk_gt_i32 s4, 0x7fff
	s_cbranch_scc0 .LBB0_1691
